# speedup vs baseline: 1.0011x; 1.0011x over previous
.LBB4_9:
	s_or_b64 exec, exec, s[22:23]
	s_waitcnt vmcnt(1)
	v_cndmask_b32_e64 v55, v54, v52, s[0:1]
	ds_bpermute_b32 v74, v62, v55
	ds_bpermute_b32 v76, v63, v55
	ds_bpermute_b32 v82, v64, v55
	ds_bpermute_b32 v86, v65, v55
	v_cvt_f32_i32_e32 v52, v70
	s_waitcnt lgkmcnt(3)
	v_ashrrev_i32_e32 v75, 31, v74
	s_waitcnt lgkmcnt(2)
	v_ashrrev_i32_e32 v77, 31, v76
	v_lshlrev_b64 v[74:75], 8, v[74:75]
	v_lshl_add_u64 v[84:85], v[50:51], 0, v[74:75]
	v_lshlrev_b64 v[74:75], 8, v[76:77]
	s_waitcnt lgkmcnt(1)
	v_ashrrev_i32_e32 v83, 31, v82
	v_lshl_add_u64 v[88:89], v[50:51], 0, v[74:75]
	global_load_dwordx4 v[74:77], v[84:85], off
	global_load_dwordx4 v[78:81], v[88:89], off
	v_lshlrev_b64 v[82:83], 8, v[82:83]
	s_waitcnt lgkmcnt(0)
	v_ashrrev_i32_e32 v87, 31, v86
	v_lshl_add_u64 v[82:83], v[50:51], 0, v[82:83]
	v_lshlrev_b64 v[86:87], 8, v[86:87]
	global_load_dwordx4 v[82:85], v[82:83], off
	v_lshl_add_u64 v[86:87], v[50:51], 0, v[86:87]
	global_load_dwordx4 v[86:89], v[86:87], off
	s_and_saveexec_b64 s[22:23], s[0:1]
	s_waitcnt vmcnt(4)
	v_cvt_f32_i32_e32 v53, v53
	v_add_f32_e32 v53, 1.0, v53
	v_mul_f32_e32 v71, 0x4b800000, v53
	v_cmp_gt_f32_e64 s[4:5], s27, v53
	s_nop 1
	v_cndmask_b32_e64 v53, v53, v71, s[4:5]
	v_rsq_f32_e32 v53, v53
	s_nop 0
	v_mul_f32_e32 v71, 0x45800000, v53
	v_cndmask_b32_e64 v53, v53, v71, s[4:5]
	s_or_b64 exec, exec, s[22:23]
	v_add_f32_e32 v52, 1.0, v52
	v_mul_f32_e32 v71, 0x4b800000, v52
	v_cmp_gt_f32_e64 s[0:1], s27, v52
	ds_bpermute_b32 v72, v62, v53
	ds_bpermute_b32 v90, v63, v53
	v_cndmask_b32_e64 v52, v52, v71, s[0:1]
	v_rsq_f32_e32 v52, v52
	ds_bpermute_b32 v92, v64, v53
	ds_bpermute_b32 v94, v65, v53
	v_mul_f32_e32 v71, 0x45800000, v52
	v_cndmask_b32_e64 v52, v52, v71, s[0:1]
	v_cmp_lt_i32_e64 s[0:1], 4, v70
	s_waitcnt vmcnt(3) lgkmcnt(3)
	v_mul_f32_e32 v76, v72, v76
	v_mul_f32_e32 v77, v72, v77
	v_mul_f32_e32 v74, v72, v74
	v_mul_f32_e32 v75, v72, v75
	v_fma_f32 v36, v36, v52, v76
	v_fma_f32 v37, v37, v52, v77
	v_fma_f32 v34, v34, v52, v74
	v_fma_f32 v35, v35, v52, v75
	s_waitcnt vmcnt(2) lgkmcnt(2)
	v_fmac_f32_e32 v36, v90, v80
	v_fmac_f32_e32 v37, v90, v81
	v_fmac_f32_e32 v34, v90, v78
	v_fmac_f32_e32 v35, v90, v79
	s_waitcnt vmcnt(1) lgkmcnt(1)
	v_fmac_f32_e32 v36, v92, v84
	v_fmac_f32_e32 v37, v92, v85
	v_fma_f32 v74, v92, v82, v34
	v_fma_f32 v75, v92, v83, v35
	s_waitcnt vmcnt(0) lgkmcnt(0)
	v_fma_f32 v34, v94, v88, v36
	v_fma_f32 v35, v94, v89, v37
	v_fma_f32 v36, v94, v86, v74
	v_fma_f32 v37, v94, v87, v75
	s_and_saveexec_b64 s[4:5], s[0:1]
	s_cbranch_execz .LBB4_13
	v_min_i32_e32 v71, 16, v70
	v_add_u32_e32 v71, -4, v71
	s_mov_b64 s[22:23], 0
	v_mov_b32_e32 v72, v66
.LBB4_11:
	ds_bpermute_b32 v74, v72, v55
	ds_bpermute_b32 v78, v72, v53
	v_add_u32_e32 v71, -1, v71
	v_cmp_eq_u32_e64 s[0:1], 0, v71
	v_add_u32_e32 v72, 4, v72
	s_waitcnt lgkmcnt(1)
	v_ashrrev_i32_e32 v75, 31, v74
	v_lshlrev_b64 v[74:75], 8, v[74:75]
	v_lshl_add_u64 v[74:75], v[50:51], 0, v[74:75]
	global_load_dwordx4 v[74:77], v[74:75], off
	s_or_b64 s[22:23], s[0:1], s[22:23]
	s_waitcnt vmcnt(0) lgkmcnt(0)
	v_fmac_f32_e32 v34, v76, v78
	v_fmac_f32_e32 v35, v77, v78
	v_fmac_f32_e32 v36, v74, v78
	v_fmac_f32_e32 v37, v75, v78
	s_andn2_b64 exec, exec, s[22:23]
	s_cbranch_execnz .LBB4_11
	s_or_b64 exec, exec, s[22:23]
